# LRU merge phase (P8): the 32 row RMS scales of an item computed once, one row per lane (8 LDS reads in flight, one sqrt/divide sequence), broadcast per row by v_readlane; replaces a per-row serial cha
# speedup vs baseline: 1.0180x; 1.0127x over previous
.LBB0_1583:
	v_mbcnt_lo_u32_b32 v54, -1, 0
	v_mbcnt_hi_u32_b32 v54, -1, v54
	v_and_b32_e32 v54, 31, v54
	v_lshlrev_b32_e32 v54, 2, v54
	v_or_b32_e32 v54, 0x20000, v54
	ds_read_b32 v46, v54
	ds_read_b32 v47, v54 offset:128
	ds_read_b32 v48, v54 offset:256
	ds_read_b32 v49, v54 offset:384
	ds_read_b32 v50, v54 offset:512
	ds_read_b32 v51, v54 offset:640
	ds_read_b32 v52, v54 offset:768
	ds_read_b32 v53, v54 offset:896
	s_waitcnt lgkmcnt(0)
	v_add_f32_e32 v45, 0, v46
	v_add_f32_e32 v45, v45, v47
	v_add_f32_e32 v45, v45, v48
	v_add_f32_e32 v45, v45, v49
	v_add_f32_e32 v45, v45, v50
	v_add_f32_e32 v45, v45, v51
	v_add_f32_e32 v45, v45, v52
	v_add_f32_e32 v45, v45, v53
	v_fmamk_f32 v45, v45, 0x3a800000, v96
	v_cmp_gt_f32_e32 vcc, s56, v45
	v_mul_f32_e32 v46, 0x4f800000, v45
	s_nop 0
	v_cndmask_b32_e32 v45, v45, v46, vcc
	v_sqrt_f32_e32 v46, v45
	s_nop 0
	v_add_u32_e32 v47, -1, v46
	v_fma_f32 v48, -v47, v46, v45
	v_cmp_ge_f32_e64 s[8:9], 0, v48
	v_add_u32_e32 v48, 1, v46
	s_nop 0
	v_cndmask_b32_e64 v47, v46, v47, s[8:9]
	v_fma_f32 v46, -v48, v46, v45
	v_cmp_lt_f32_e64 s[8:9], 0, v46
	s_nop 1
	v_cndmask_b32_e64 v46, v47, v48, s[8:9]
	v_mul_f32_e32 v47, 0x37800000, v46
	v_cndmask_b32_e32 v46, v46, v47, vcc
	v_cmp_class_f32_e32 vcc, v45, v97
	s_nop 1
	v_cndmask_b32_e32 v45, v46, v45, vcc
	v_div_scale_f32 v46, s[8:9], v45, v45, 1.0
	v_rcp_f32_e32 v47, v46
	s_nop 0
	v_fma_f32 v48, -v46, v47, 1.0
	v_fmac_f32_e32 v47, v48, v47
	v_div_scale_f32 v48, vcc, 1.0, v45, 1.0
	v_mul_f32_e32 v49, v48, v47
	v_fma_f32 v50, -v46, v49, v48
	v_fmac_f32_e32 v49, v50, v47
	v_fma_f32 v46, -v46, v49, v48
	v_div_fmas_f32 v46, v46, v47, v49
	v_div_fixup_f32 v45, v46, v45, 1.0
	ds_read2st64_b64 v[46:49], v44 offset1:8
	ds_read2st64_b64 v[50:53], v44 offset0:16 offset1:24
	v_add_co_u32_e32 v54, vcc, s43, v42
	v_readlane_b32 s8, v45, 0
	v_readlane_b32 s9, v45, 1
	v_addc_co_u32_e32 v55, vcc, -1, v43, vcc
	v_readlane_b32 s14, v45, 2
	v_readlane_b32 s15, v45, 3
	v_add_u32_e32 v44, 0x4000, v44
	s_waitcnt lgkmcnt(1)
	v_mul_f32_e32 v46, s8, v46
	v_mul_f32_e32 v47, s8, v47
	v_mul_f32_e32 v46, v32, v46
	v_mul_f32_e32 v47, v33, v47
	v_cvt_pk_bf16_f32 v46, v46, v47
	v_mul_f32_e32 v48, s9, v48
	v_mul_f32_e32 v49, s9, v49
	v_mul_f32_e32 v48, v32, v48
	v_mul_f32_e32 v49, v33, v49
	v_cvt_pk_bf16_f32 v48, v48, v49
	global_store_dword v[54:55], v46, off offset:-4096
	global_store_dword v[54:55], v48, off
	s_waitcnt lgkmcnt(0)
	v_mul_f32_e32 v50, s14, v50
	v_mul_f32_e32 v51, s14, v51
	v_mul_f32_e32 v50, v32, v50
	v_mul_f32_e32 v51, v33, v51
	v_cvt_pk_bf16_f32 v50, v50, v51
	v_mul_f32_e32 v52, s15, v52
	v_mul_f32_e32 v53, s15, v53
	v_mul_f32_e32 v52, v32, v52
	v_mul_f32_e32 v53, v33, v53
	v_cvt_pk_bf16_f32 v52, v52, v53
	global_store_dword v[42:43], v50, off offset:-4096
	global_store_dword v[42:43], v52, off
	v_lshl_add_u64 v[42:43], v[42:43], 0, s[10:11]
	ds_read2st64_b64 v[46:49], v44 offset1:8
	ds_read2st64_b64 v[50:53], v44 offset0:16 offset1:24
	v_add_co_u32_e32 v54, vcc, s43, v42
	v_readlane_b32 s8, v45, 4
	v_readlane_b32 s9, v45, 5
	v_addc_co_u32_e32 v55, vcc, -1, v43, vcc
	v_readlane_b32 s14, v45, 6
	v_readlane_b32 s15, v45, 7
	v_add_u32_e32 v44, 0x4000, v44
	s_waitcnt lgkmcnt(1)
	v_mul_f32_e32 v46, s8, v46
	v_mul_f32_e32 v47, s8, v47
	v_mul_f32_e32 v46, v32, v46
	v_mul_f32_e32 v47, v33, v47
	v_cvt_pk_bf16_f32 v46, v46, v47
	v_mul_f32_e32 v48, s9, v48
	v_mul_f32_e32 v49, s9, v49
	v_mul_f32_e32 v48, v32, v48
	v_mul_f32_e32 v49, v33, v49
	v_cvt_pk_bf16_f32 v48, v48, v49
	global_store_dword v[54:55], v46, off offset:-4096
	global_store_dword v[54:55], v48, off
	s_waitcnt lgkmcnt(0)
	v_mul_f32_e32 v50, s14, v50
	v_mul_f32_e32 v51, s14, v51
	v_mul_f32_e32 v50, v32, v50
	v_mul_f32_e32 v51, v33, v51
	v_cvt_pk_bf16_f32 v50, v50, v51
	v_mul_f32_e32 v52, s15, v52
	v_mul_f32_e32 v53, s15, v53
	v_mul_f32_e32 v52, v32, v52
	v_mul_f32_e32 v53, v33, v53
	v_cvt_pk_bf16_f32 v52, v52, v53
	global_store_dword v[42:43], v50, off offset:-4096
	global_store_dword v[42:43], v52, off
	v_lshl_add_u64 v[42:43], v[42:43], 0, s[10:11]
	ds_read2st64_b64 v[46:49], v44 offset1:8
	ds_read2st64_b64 v[50:53], v44 offset0:16 offset1:24
	v_add_co_u32_e32 v54, vcc, s43, v42
	v_readlane_b32 s8, v45, 8
	v_readlane_b32 s9, v45, 9
	v_addc_co_u32_e32 v55, vcc, -1, v43, vcc
	v_readlane_b32 s14, v45, 10
	v_readlane_b32 s15, v45, 11
	v_add_u32_e32 v44, 0x4000, v44
	s_waitcnt lgkmcnt(1)
	v_mul_f32_e32 v46, s8, v46
	v_mul_f32_e32 v47, s8, v47
	v_mul_f32_e32 v46, v32, v46
	v_mul_f32_e32 v47, v33, v47
	v_cvt_pk_bf16_f32 v46, v46, v47
	v_mul_f32_e32 v48, s9, v48
	v_mul_f32_e32 v49, s9, v49
	v_mul_f32_e32 v48, v32, v48
	v_mul_f32_e32 v49, v33, v49
	v_cvt_pk_bf16_f32 v48, v48, v49
	global_store_dword v[54:55], v46, off offset:-4096
	global_store_dword v[54:55], v48, off
	s_waitcnt lgkmcnt(0)
	v_mul_f32_e32 v50, s14, v50
	v_mul_f32_e32 v51, s14, v51
	v_mul_f32_e32 v50, v32, v50
	v_mul_f32_e32 v51, v33, v51
	v_cvt_pk_bf16_f32 v50, v50, v51
	v_mul_f32_e32 v52, s15, v52
	v_mul_f32_e32 v53, s15, v53
	v_mul_f32_e32 v52, v32, v52
	v_mul_f32_e32 v53, v33, v53
	v_cvt_pk_bf16_f32 v52, v52, v53
	global_store_dword v[42:43], v50, off offset:-4096
	global_store_dword v[42:43], v52, off
	v_lshl_add_u64 v[42:43], v[42:43], 0, s[10:11]
	ds_read2st64_b64 v[46:49], v44 offset1:8
	ds_read2st64_b64 v[50:53], v44 offset0:16 offset1:24
	v_add_co_u32_e32 v54, vcc, s43, v42
	v_readlane_b32 s8, v45, 12
	v_readlane_b32 s9, v45, 13
	v_addc_co_u32_e32 v55, vcc, -1, v43, vcc
	v_readlane_b32 s14, v45, 14
	v_readlane_b32 s15, v45, 15
	v_add_u32_e32 v44, 0x4000, v44
	s_waitcnt lgkmcnt(1)
	v_mul_f32_e32 v46, s8, v46
	v_mul_f32_e32 v47, s8, v47
	v_mul_f32_e32 v46, v32, v46
	v_mul_f32_e32 v47, v33, v47
	v_cvt_pk_bf16_f32 v46, v46, v47
	v_mul_f32_e32 v48, s9, v48
	v_mul_f32_e32 v49, s9, v49
	v_mul_f32_e32 v48, v32, v48
	v_mul_f32_e32 v49, v33, v49
	v_cvt_pk_bf16_f32 v48, v48, v49
	global_store_dword v[54:55], v46, off offset:-4096
	global_store_dword v[54:55], v48, off
	s_waitcnt lgkmcnt(0)
	v_mul_f32_e32 v50, s14, v50
	v_mul_f32_e32 v51, s14, v51
	v_mul_f32_e32 v50, v32, v50
	v_mul_f32_e32 v51, v33, v51
	v_cvt_pk_bf16_f32 v50, v50, v51
	v_mul_f32_e32 v52, s15, v52
	v_mul_f32_e32 v53, s15, v53
	v_mul_f32_e32 v52, v32, v52
	v_mul_f32_e32 v53, v33, v53
	v_cvt_pk_bf16_f32 v52, v52, v53
	global_store_dword v[42:43], v50, off offset:-4096
	global_store_dword v[42:43], v52, off
	v_lshl_add_u64 v[42:43], v[42:43], 0, s[10:11]
	ds_read2st64_b64 v[46:49], v44 offset1:8
	ds_read2st64_b64 v[50:53], v44 offset0:16 offset1:24
	v_add_co_u32_e32 v54, vcc, s43, v42
	v_readlane_b32 s8, v45, 16
	v_readlane_b32 s9, v45, 17
	v_addc_co_u32_e32 v55, vcc, -1, v43, vcc
	v_readlane_b32 s14, v45, 18
	v_readlane_b32 s15, v45, 19
	v_add_u32_e32 v44, 0x4000, v44
	s_waitcnt lgkmcnt(1)
	v_mul_f32_e32 v46, s8, v46
	v_mul_f32_e32 v47, s8, v47
	v_mul_f32_e32 v46, v32, v46
	v_mul_f32_e32 v47, v33, v47
	v_cvt_pk_bf16_f32 v46, v46, v47
	v_mul_f32_e32 v48, s9, v48
	v_mul_f32_e32 v49, s9, v49
	v_mul_f32_e32 v48, v32, v48
	v_mul_f32_e32 v49, v33, v49
	v_cvt_pk_bf16_f32 v48, v48, v49
	global_store_dword v[54:55], v46, off offset:-4096
	global_store_dword v[54:55], v48, off
	s_waitcnt lgkmcnt(0)
	v_mul_f32_e32 v50, s14, v50
	v_mul_f32_e32 v51, s14, v51
	v_mul_f32_e32 v50, v32, v50
	v_mul_f32_e32 v51, v33, v51
	v_cvt_pk_bf16_f32 v50, v50, v51
	v_mul_f32_e32 v52, s15, v52
	v_mul_f32_e32 v53, s15, v53
	v_mul_f32_e32 v52, v32, v52
	v_mul_f32_e32 v53, v33, v53
	v_cvt_pk_bf16_f32 v52, v52, v53
	global_store_dword v[42:43], v50, off offset:-4096
	global_store_dword v[42:43], v52, off
	v_lshl_add_u64 v[42:43], v[42:43], 0, s[10:11]
	ds_read2st64_b64 v[46:49], v44 offset1:8
	ds_read2st64_b64 v[50:53], v44 offset0:16 offset1:24
	v_add_co_u32_e32 v54, vcc, s43, v42
	v_readlane_b32 s8, v45, 20
	v_readlane_b32 s9, v45, 21
	v_addc_co_u32_e32 v55, vcc, -1, v43, vcc
	v_readlane_b32 s14, v45, 22
	v_readlane_b32 s15, v45, 23
	v_add_u32_e32 v44, 0x4000, v44
	s_waitcnt lgkmcnt(1)
	v_mul_f32_e32 v46, s8, v46
	v_mul_f32_e32 v47, s8, v47
	v_mul_f32_e32 v46, v32, v46
	v_mul_f32_e32 v47, v33, v47
	v_cvt_pk_bf16_f32 v46, v46, v47
	v_mul_f32_e32 v48, s9, v48
	v_mul_f32_e32 v49, s9, v49
	v_mul_f32_e32 v48, v32, v48
	v_mul_f32_e32 v49, v33, v49
	v_cvt_pk_bf16_f32 v48, v48, v49
	global_store_dword v[54:55], v46, off offset:-4096
	global_store_dword v[54:55], v48, off
	s_waitcnt lgkmcnt(0)
	v_mul_f32_e32 v50, s14, v50
	v_mul_f32_e32 v51, s14, v51
	v_mul_f32_e32 v50, v32, v50
	v_mul_f32_e32 v51, v33, v51
	v_cvt_pk_bf16_f32 v50, v50, v51
	v_mul_f32_e32 v52, s15, v52
	v_mul_f32_e32 v53, s15, v53
	v_mul_f32_e32 v52, v32, v52
	v_mul_f32_e32 v53, v33, v53
	v_cvt_pk_bf16_f32 v52, v52, v53
	global_store_dword v[42:43], v50, off offset:-4096
	global_store_dword v[42:43], v52, off
	v_lshl_add_u64 v[42:43], v[42:43], 0, s[10:11]
	ds_read2st64_b64 v[46:49], v44 offset1:8
	ds_read2st64_b64 v[50:53], v44 offset0:16 offset1:24
	v_add_co_u32_e32 v54, vcc, s43, v42
	v_readlane_b32 s8, v45, 24
	v_readlane_b32 s9, v45, 25
	v_addc_co_u32_e32 v55, vcc, -1, v43, vcc
	v_readlane_b32 s14, v45, 26
	v_readlane_b32 s15, v45, 27
	v_add_u32_e32 v44, 0x4000, v44
	s_waitcnt lgkmcnt(1)
	v_mul_f32_e32 v46, s8, v46
	v_mul_f32_e32 v47, s8, v47
	v_mul_f32_e32 v46, v32, v46
	v_mul_f32_e32 v47, v33, v47
	v_cvt_pk_bf16_f32 v46, v46, v47
	v_mul_f32_e32 v48, s9, v48
	v_mul_f32_e32 v49, s9, v49
	v_mul_f32_e32 v48, v32, v48
	v_mul_f32_e32 v49, v33, v49
	v_cvt_pk_bf16_f32 v48, v48, v49
	global_store_dword v[54:55], v46, off offset:-4096
	global_store_dword v[54:55], v48, off
	s_waitcnt lgkmcnt(0)
	v_mul_f32_e32 v50, s14, v50
	v_mul_f32_e32 v51, s14, v51
	v_mul_f32_e32 v50, v32, v50
	v_mul_f32_e32 v51, v33, v51
	v_cvt_pk_bf16_f32 v50, v50, v51
	v_mul_f32_e32 v52, s15, v52
	v_mul_f32_e32 v53, s15, v53
	v_mul_f32_e32 v52, v32, v52
	v_mul_f32_e32 v53, v33, v53
	v_cvt_pk_bf16_f32 v52, v52, v53
	global_store_dword v[42:43], v50, off offset:-4096
	global_store_dword v[42:43], v52, off
	v_lshl_add_u64 v[42:43], v[42:43], 0, s[10:11]
	ds_read2st64_b64 v[46:49], v44 offset1:8
	ds_read2st64_b64 v[50:53], v44 offset0:16 offset1:24
	v_add_co_u32_e32 v54, vcc, s43, v42
	v_readlane_b32 s8, v45, 28
	v_readlane_b32 s9, v45, 29
	v_addc_co_u32_e32 v55, vcc, -1, v43, vcc
	v_readlane_b32 s14, v45, 30
	v_readlane_b32 s15, v45, 31
	v_add_u32_e32 v44, 0x4000, v44
	s_waitcnt lgkmcnt(1)
	v_mul_f32_e32 v46, s8, v46
	v_mul_f32_e32 v47, s8, v47
	v_mul_f32_e32 v46, v32, v46
	v_mul_f32_e32 v47, v33, v47
	v_cvt_pk_bf16_f32 v46, v46, v47
	v_mul_f32_e32 v48, s9, v48
	v_mul_f32_e32 v49, s9, v49
	v_mul_f32_e32 v48, v32, v48
	v_mul_f32_e32 v49, v33, v49
	v_cvt_pk_bf16_f32 v48, v48, v49
	global_store_dword v[54:55], v46, off offset:-4096
	global_store_dword v[54:55], v48, off
	s_waitcnt lgkmcnt(0)
	v_mul_f32_e32 v50, s14, v50
	v_mul_f32_e32 v51, s14, v51
	v_mul_f32_e32 v50, v32, v50
	v_mul_f32_e32 v51, v33, v51
	v_cvt_pk_bf16_f32 v50, v50, v51
	v_mul_f32_e32 v52, s15, v52
	v_mul_f32_e32 v53, s15, v53
	v_mul_f32_e32 v52, v32, v52
	v_mul_f32_e32 v53, v33, v53
	v_cvt_pk_bf16_f32 v52, v52, v53
	global_store_dword v[42:43], v50, off offset:-4096
	global_store_dword v[42:43], v52, off
	v_lshl_add_u64 v[42:43], v[42:43], 0, s[10:11]
	s_barrier
	s_load_dword s8, s[90:91], 0x100
	s_andn2_b64 vcc, exec, s[12:13]
	s_mov_b32 s14, s59
	s_waitcnt lgkmcnt(0)
	s_add_i32 s57, s57, s8
	s_cbranch_vccnz .LBB0_1518
	v_readlane_b32 s52, v254, 10
